# prep token-shift staging: cur/prv/mu loads of all 9-10 blocks hoisted into block 0 (fixed offsets), later serialized loads become register moves
# speedup vs baseline: 1.0043x; 1.0043x over previous
.LBB0_269:
	s_or_b64 exec, exec, s[4:5]
	v_mov_b32_e32 v0, s2
	v_mbcnt_lo_u32_b32 v104, -1, 0
	v_mbcnt_hi_u32_b32 v104, -1, v104
	v_readlane_b32 s0, v254, 0
	v_readfirstlane_b32 s62, v0
	v_mov_b32_e32 v0, 0
	v_add_u32_e32 v106, s0, v104
	v_readfirstlane_b32 s70, v0
	s_ashr_i32 s71, s70, 31
	s_waitcnt lgkmcnt(0)
	s_add_u32 s54, s60, s70
	s_addc_u32 s55, s61, s71
	s_add_u32 s58, s54, 0x37c80000
	s_addc_u32 s59, s55, 0
	s_lshl_b32 s33, s62, 5
	v_ashrrev_i32_e32 v109, 4, v106
	v_add_u32_e32 v8, s33, v109
	s_movk_i32 s0, 0x3400
	v_mov_b64_e32 v[0:1], s[58:59]
	v_mad_i64_i32 v[0:1], s[4:5], v8, s0, v[0:1]
	v_lshlrev_b32_e32 v176, 1, v104
	s_mov_b64 s[4:5], 0x1800
	v_and_b32_e32 v11, 30, v176
	v_lshl_add_u64 v[2:3], v[0:1], 0, s[4:5]
	v_lshlrev_b32_e32 v4, 1, v11
	v_lshl_add_u64 v[6:7], v[2:3], 0, v[4:5]
	global_load_dword v10, v[6:7], off
	global_load_dword v202, v[6:7], off offset:128
	global_load_dword v203, v[6:7], off offset:192
	global_load_dword v204, v[6:7], off offset:256
	global_load_dword v205, v[6:7], off offset:320
	global_load_dword v206, v[6:7], off offset:384
	global_load_dword v207, v[6:7], off offset:448
	global_load_dword v208, v[6:7], off offset:512
	v_writelane_b32 v254, s12, 18
	s_load_dwordx4 s[36:39], s[12:13], 0x30
	s_movk_i32 s4, 0xe400
	v_and_b32_e32 v6, 0x7ff, v8
	s_mov_b32 s5, -1
	v_cmp_ne_u32_e32 vcc, 0, v6
	v_lshl_add_u64 v[0:1], v[0:1], 0, s[4:5]
	v_writelane_b32 v254, s13, 19
	s_and_saveexec_b64 s[4:5], vcc
	s_cbranch_execz .LBB0_271
	v_mov_b32_e32 v5, 0
	v_lshl_add_u64 v[6:7], v[0:1], 0, v[4:5]
	global_load_dword v5, v[6:7], off
	global_load_dword v211, v[6:7], off offset:64
	global_load_dword v212, v[6:7], off offset:128
	global_load_dword v213, v[6:7], off offset:192
	global_load_dword v214, v[6:7], off offset:256
	global_load_dword v215, v[6:7], off offset:320
	global_load_dword v216, v[6:7], off offset:384
	global_load_dword v217, v[6:7], off offset:448
	global_load_dword v218, v[6:7], off offset:512
.LBB0_271:
	s_or_b64 exec, exec, s[4:5]
	s_waitcnt lgkmcnt(0)
	s_add_u32 s4, s36, 0x3000
	s_addc_u32 s5, s37, 0
	v_lshlrev_b32_e32 v6, 2, v11
	global_load_dwordx2 v[12:13], v6, s[4:5]
	global_load_dwordx2 v[222:223], v6, s[4:5] offset:128
	global_load_dwordx2 v[224:225], v6, s[4:5] offset:256
	global_load_dwordx2 v[226:227], v6, s[4:5] offset:384
	global_load_dwordx2 v[228:229], v6, s[4:5] offset:512
	global_load_dwordx2 v[230:231], v6, s[4:5] offset:640
	global_load_dwordx2 v[232:233], v6, s[4:5] offset:768
	global_load_dwordx2 v[234:235], v6, s[4:5] offset:896
	global_load_dwordx2 v[236:237], v6, s[4:5] offset:1024
	v_or_b32_e32 v8, 32, v11
	v_mov_b32_e32 v7, 0
	v_lshlrev_b32_e32 v6, 1, v8
	v_lshl_add_u64 v[14:15], v[2:3], 0, v[6:7]
	global_load_dword v9, v[14:15], off
	s_waitcnt vmcnt(0)
	v_lshlrev_b32_e32 v14, 16, v10
	v_lshlrev_b32_e32 v15, 16, v5
	v_and_b32_e32 v10, 0xffff0000, v10
	v_and_b32_e32 v5, 0xffff0000, v5
	v_sub_f32_e32 v15, v15, v14
	v_sub_f32_e32 v5, v5, v10
	v_readlane_b32 s0, v254, 18
	v_readlane_b32 s1, v254, 19
	s_load_dwordx2 s[72:73], s[0:1], 0x70
	s_load_dwordx4 s[40:43], s[0:1], 0x60
	s_load_dwordx2 s[74:75], s[0:1], 0x48
	s_movk_i32 s0, 0x290
	s_waitcnt vmcnt(1)
	v_fmac_f32_e32 v14, v12, v15
	v_fmac_f32_e32 v10, v13, v5
	v_add_f32_e32 v5, v14, v14
	v_add_f32_e32 v10, v10, v10
	v_mul_f32_e32 v5, 0x3fb8aa3b, v5
	v_mul_f32_e32 v10, 0x3fb8aa3b, v10
	v_exp_f32_e32 v5, v5
	v_exp_f32_e32 v10, v10
	v_mov_b32_e32 v13, 0
	v_add_f32_e32 v5, 1.0, v5
	v_add_f32_e32 v10, 1.0, v10
	v_rcp_f32_e32 v14, v5
	v_rcp_f32_e32 v15, v10
	v_mul_lo_u32 v5, v109, s0
	v_add_u32_e32 v12, 0, v5
	v_add_u32_e32 v10, v12, v4
	v_pk_fma_f32 v[4:5], v[14:15], -2.0, 1.0 op_sel_hi:[1,0,0]
	s_nop 0
	v_cvt_pk_bf16_f32 v4, v4, v5
	ds_write_b32 v10, v4
	s_and_saveexec_b64 s[6:7], vcc
	s_cbranch_execz .LBB0_273
	v_mov_b32_e32 v5, 0
	v_mov_b32_e32 v4, v6
	v_lshl_add_u64 v[4:5], v[0:1], 0, v[4:5]
	v_mov_b32_e32 v13, v211
.LBB0_273:
	s_or_b64 exec, exec, s[6:7]
	v_lshlrev_b32_e32 v4, 2, v8
	v_mov_b64_e32 v[14:15], v[222:223]
	v_or_b32_e32 v4, 64, v11
	v_lshlrev_b32_e32 v6, 1, v4
	v_lshl_add_u64 v[16:17], v[2:3], 0, v[6:7]
	v_mov_b32_e32 v5, v202
	s_waitcnt vmcnt(2)
	v_lshlrev_b32_e32 v16, 16, v9
	v_lshlrev_b32_e32 v17, 16, v13
	v_and_b32_e32 v9, 0xffff0000, v9
	v_and_b32_e32 v13, 0xffff0000, v13
	v_sub_f32_e32 v17, v17, v16
	v_sub_f32_e32 v13, v13, v9
	v_lshl_add_u32 v8, v8, 1, v12
	s_waitcnt vmcnt(1)
	v_fmac_f32_e32 v16, v14, v17
	v_fmac_f32_e32 v9, v15, v13
	v_add_f32_e32 v13, v16, v16
	v_add_f32_e32 v9, v9, v9
	v_mul_f32_e32 v13, 0x3fb8aa3b, v13
	v_mul_f32_e32 v9, 0x3fb8aa3b, v9
	v_exp_f32_e32 v13, v13
	v_exp_f32_e32 v9, v9
	v_add_f32_e32 v13, 1.0, v13
	v_add_f32_e32 v9, 1.0, v9
	v_rcp_f32_e32 v14, v13
	v_rcp_f32_e32 v15, v9
	s_nop 0
	v_pk_fma_f32 v[14:15], v[14:15], -2.0, 1.0 op_sel_hi:[1,0,0]
	s_nop 0
	v_cvt_pk_bf16_f32 v9, v14, v15
	ds_write_b32 v8, v9
	s_and_saveexec_b64 s[6:7], vcc
	s_cbranch_execz .LBB0_275
	v_mov_b32_e32 v7, 0
	v_lshl_add_u64 v[6:7], v[0:1], 0, v[6:7]
	v_mov_b32_e32 v7, v212
.LBB0_275:
	s_or_b64 exec, exec, s[6:7]
	v_lshlrev_b32_e32 v6, 2, v4
	v_mov_b64_e32 v[14:15], v[224:225]
	v_or_b32_e32 v6, 0x60, v11
	v_mov_b32_e32 v9, 0
	v_lshlrev_b32_e32 v8, 1, v6
	v_lshl_add_u64 v[16:17], v[2:3], 0, v[8:9]
	v_mov_b32_e32 v13, v203
	s_waitcnt vmcnt(2)
	v_lshlrev_b32_e32 v16, 16, v5
	v_lshlrev_b32_e32 v18, 16, v7
	v_and_b32_e32 v17, 0xffff0000, v5
	v_and_b32_e32 v19, 0xffff0000, v7
	v_lshl_add_u32 v7, v4, 1, v12
	v_pk_add_f32 v[4:5], v[18:19], v[16:17] neg_lo:[0,1] neg_hi:[0,1]
	s_waitcnt vmcnt(1)
	v_pk_fma_f32 v[4:5], v[14:15], v[4:5], v[16:17]
	s_nop 0
	v_cvt_pk_bf16_f32 v4, v4, v5
	ds_write_b32 v7, v4
	v_mov_b32_e32 v4, 0
	s_and_saveexec_b64 s[6:7], vcc
	s_cbranch_execz .LBB0_277
	v_mov_b32_e32 v5, 0
	v_mov_b32_e32 v4, v8
	v_lshl_add_u64 v[4:5], v[0:1], 0, v[4:5]
	v_mov_b32_e32 v4, v213
.LBB0_277:
	s_or_b64 exec, exec, s[6:7]
	v_lshlrev_b32_e32 v5, 2, v6
	v_or_b32_e32 v7, 0x80, v11
	v_mov_b64_e32 v[16:17], v[226:227]
	v_lshlrev_b32_e32 v8, 1, v7
	v_lshl_add_u64 v[14:15], v[2:3], 0, v[8:9]
	v_mov_b32_e32 v14, v204
	s_waitcnt vmcnt(2)
	v_lshlrev_b32_e32 v18, 16, v13
	v_lshlrev_b32_e32 v20, 16, v4
	v_and_b32_e32 v19, 0xffff0000, v13
	v_and_b32_e32 v21, 0xffff0000, v4
	v_pk_add_f32 v[4:5], v[20:21], v[18:19] neg_lo:[0,1] neg_hi:[0,1]
	s_waitcnt vmcnt(1)
	v_pk_fma_f32 v[4:5], v[16:17], v[4:5], v[18:19]
	s_nop 0
	v_cvt_pk_bf16_f32 v4, v4, v5
	v_lshl_add_u32 v5, v6, 1, v12
	ds_write_b32 v5, v4
	s_and_saveexec_b64 s[6:7], vcc
	s_cbranch_execz .LBB0_279
	v_mov_b32_e32 v9, 0
	v_lshl_add_u64 v[4:5], v[0:1], 0, v[8:9]
	v_mov_b32_e32 v9, v214
.LBB0_279:
	s_or_b64 exec, exec, s[6:7]
	v_lshlrev_b32_e32 v4, 2, v7
	v_mov_b64_e32 v[16:17], v[228:229]
	v_or_b32_e32 v6, 0xa0, v11
	v_mov_b32_e32 v5, 0
	v_lshlrev_b32_e32 v4, 1, v6
	v_lshl_add_u64 v[18:19], v[2:3], 0, v[4:5]
	v_mov_b32_e32 v13, v205
	s_waitcnt vmcnt(2)
	v_lshlrev_b32_e32 v8, 16, v14
	v_lshlrev_b32_e32 v15, 16, v9
	v_and_b32_e32 v14, 0xffff0000, v14
	v_and_b32_e32 v9, 0xffff0000, v9
	v_sub_f32_e32 v15, v15, v8
	v_sub_f32_e32 v9, v9, v14
	v_lshl_add_u32 v7, v7, 1, v12
	s_waitcnt vmcnt(1)
	v_fmac_f32_e32 v8, v16, v15
	v_fmac_f32_e32 v14, v17, v9
	v_mul_f32_e32 v8, 0xbfb8aa3b, v8
	v_mul_f32_e32 v9, 0xbfb8aa3b, v14
	v_exp_f32_e32 v8, v8
	v_exp_f32_e32 v9, v9
	v_add_f32_e32 v8, 1.0, v8
	v_add_f32_e32 v9, 1.0, v9
	v_rcp_f32_e32 v8, v8
	v_rcp_f32_e32 v9, v9
	s_nop 0
	v_cvt_pk_bf16_f32 v8, v8, v9
	ds_write_b32 v7, v8
	v_mov_b32_e32 v7, 0
	s_and_saveexec_b64 s[6:7], vcc
	s_cbranch_execz .LBB0_281
	v_mov_b32_e32 v9, 0
	v_mov_b32_e32 v8, v4
	v_lshl_add_u64 v[8:9], v[0:1], 0, v[8:9]
	v_mov_b32_e32 v7, v215
.LBB0_281:
	s_or_b64 exec, exec, s[6:7]
	v_lshlrev_b32_e32 v4, 2, v6
	v_mov_b64_e32 v[14:15], v[230:231]
	v_or_b32_e32 v8, 0xc0, v11
	v_lshlrev_b32_e32 v4, 1, v8
	v_lshl_add_u64 v[16:17], v[2:3], 0, v[4:5]
	v_mov_b32_e32 v9, v206
	s_waitcnt vmcnt(2)
	v_lshlrev_b32_e32 v16, 16, v13
	v_lshlrev_b32_e32 v17, 16, v7
	v_and_b32_e32 v13, 0xffff0000, v13
	v_and_b32_e32 v7, 0xffff0000, v7
	v_sub_f32_e32 v17, v17, v16
	v_sub_f32_e32 v7, v7, v13
	v_lshl_add_u32 v6, v6, 1, v12
	s_waitcnt vmcnt(1)
	v_fmac_f32_e32 v16, v14, v17
	v_fmac_f32_e32 v13, v15, v7
	v_mul_f32_e32 v7, 0xbfb8aa3b, v16
	v_mul_f32_e32 v13, 0xbfb8aa3b, v13
	v_exp_f32_e32 v7, v7
	v_exp_f32_e32 v13, v13
	v_add_f32_e32 v7, 1.0, v7
	v_add_f32_e32 v13, 1.0, v13
	v_rcp_f32_e32 v7, v7
	v_rcp_f32_e32 v13, v13
	s_nop 0
	v_cvt_pk_bf16_f32 v7, v7, v13
	ds_write_b32 v6, v7
	s_and_saveexec_b64 s[6:7], vcc
	s_cbranch_execz .LBB0_283
	v_mov_b32_e32 v5, 0
	v_lshl_add_u64 v[4:5], v[0:1], 0, v[4:5]
	v_mov_b32_e32 v5, v216
.LBB0_283:
	s_or_b64 exec, exec, s[6:7]
	v_lshlrev_b32_e32 v4, 2, v8
	v_mov_b64_e32 v[14:15], v[232:233]
	v_or_b32_e32 v4, 0xe0, v11
	v_mov_b32_e32 v7, 0
	v_lshlrev_b32_e32 v6, 1, v4
	v_lshl_add_u64 v[16:17], v[2:3], 0, v[6:7]
	v_mov_b32_e32 v13, v207
	s_waitcnt vmcnt(2)
	v_lshlrev_b32_e32 v16, 16, v9
	v_lshlrev_b32_e32 v17, 16, v5
	v_and_b32_e32 v9, 0xffff0000, v9
	v_and_b32_e32 v5, 0xffff0000, v5
	v_sub_f32_e32 v17, v17, v16
	v_sub_f32_e32 v5, v5, v9
	v_lshl_add_u32 v8, v8, 1, v12
	s_waitcnt vmcnt(1)
	v_fmac_f32_e32 v16, v14, v17
	v_fmac_f32_e32 v9, v15, v5
	v_mul_f32_e32 v5, 0xbfb8aa3b, v16
	v_mul_f32_e32 v9, 0xbfb8aa3b, v9
	v_exp_f32_e32 v5, v5
	v_exp_f32_e32 v9, v9
	v_add_f32_e32 v5, 1.0, v5
	v_add_f32_e32 v9, 1.0, v9
	v_rcp_f32_e32 v5, v5
	v_rcp_f32_e32 v9, v9
	s_nop 0
	v_cvt_pk_bf16_f32 v5, v5, v9
	ds_write_b32 v8, v5
	v_mov_b32_e32 v8, 0
	s_and_saveexec_b64 s[6:7], vcc
	s_cbranch_execz .LBB0_285
	v_mov_b32_e32 v9, 0
	v_mov_b32_e32 v8, v6
	v_lshl_add_u64 v[8:9], v[0:1], 0, v[8:9]
	v_mov_b32_e32 v8, v217
.LBB0_285:
	v_writelane_b32 v254, s49, 20
	s_or_b64 exec, exec, s[6:7]
	v_lshlrev_b32_e32 v5, 2, v4
	v_mov_b64_e32 v[14:15], v[234:235]
	v_or_b32_e32 v5, 0x100, v11
	v_lshlrev_b32_e32 v6, 1, v5
	v_lshl_add_u64 v[2:3], v[2:3], 0, v[6:7]
	v_mov_b32_e32 v2, v208
	s_waitcnt vmcnt(2)
	v_lshlrev_b32_e32 v3, 16, v13
	v_lshlrev_b32_e32 v9, 16, v8
	v_and_b32_e32 v11, 0xffff0000, v13
	v_and_b32_e32 v8, 0xffff0000, v8
	v_sub_f32_e32 v9, v9, v3
	v_sub_f32_e32 v8, v8, v11
	v_lshl_add_u32 v4, v4, 1, v12
	s_waitcnt vmcnt(1)
	v_fmac_f32_e32 v3, v14, v9
	v_fmac_f32_e32 v11, v15, v8
	v_mul_f32_e32 v3, 0xbfb8aa3b, v3
	v_mul_f32_e32 v8, 0xbfb8aa3b, v11
	v_exp_f32_e32 v3, v3
	v_exp_f32_e32 v8, v8
	v_add_f32_e32 v3, 1.0, v3
	v_add_f32_e32 v8, 1.0, v8
	v_rcp_f32_e32 v3, v3
	v_rcp_f32_e32 v8, v8
	s_nop 0
	v_cvt_pk_bf16_f32 v3, v3, v8
	ds_write_b32 v4, v3
	s_and_saveexec_b64 s[6:7], vcc
	s_cbranch_execz .LBB0_287
	v_mov_b32_e32 v7, 0
	v_lshl_add_u64 v[0:1], v[0:1], 0, v[6:7]
	v_mov_b32_e32 v7, v218
.LBB0_287:
	s_or_b64 exec, exec, s[6:7]
	v_lshlrev_b32_e32 v0, 2, v5
	v_mov_b64_e32 v[8:9], v[236:237]
	s_add_u32 s76, s54, 0x48480000
	s_addc_u32 s77, s55, 0
	s_waitcnt vmcnt(1)
	v_lshlrev_b32_e32 v1, 16, v2
	v_lshlrev_b32_e32 v3, 16, v7
	v_and_b32_e32 v11, 0xffff0000, v2
	v_and_b32_e32 v2, 0xffff0000, v7
	v_lshl_add_u32 v12, v5, 1, v12
	v_mov_b32_e32 v4, 0
	v_ashrrev_i32_e32 v5, 4, v104
	v_min_i32_e32 v7, 0x197, v104
	s_mov_b32 s30, 0x2aaaaaab
	s_add_u32 s78, s54, 0x33c80000
	s_mul_i32 s0, s48, 0x2400
	v_lshlrev_b32_e32 v6, 2, v104
	ds_write_b32 v10, v4 offset:576
	v_lshlrev_b32_e32 v110, 3, v5
	v_mul_hi_i32 v4, v7, s30
	s_addc_u32 s79, s55, 0
	s_lshl_b32 s56, s48, 4
	v_sub_f32_e32 v14, v2, v11
	v_lshlrev_b32_e32 v2, 2, v5
	v_xor_b32_e32 v107, 64, v6
	v_xor_b32_e32 v178, 0x80, v6
	v_add_u32_e32 v5, 23, v7
	v_ashrrev_i32_e32 v111, 31, v110
	v_lshrrev_b32_e32 v6, 31, v4
	v_ashrrev_i32_e32 v16, 2, v4
	s_add_i32 s49, s0, 0
	s_lshl_b32 s0, s48, 1
	v_writelane_b32 v254, s48, 21
	s_and_b32 s47, s56, 16
	v_and_b32_e32 v177, 15, v104
	s_mov_b64 s[8:9], 0x540000
	v_cmp_gt_u32_e64 s[4:5], 47, v5
	v_lshl_add_u64 v[4:5], v[110:111], 1, s[54:55]
	v_add_u32_e32 v16, v16, v6
	v_writelane_b32 v254, s0, 22
	s_and_b32 s46, s0, 0x7fffffc
	s_or_b32 s0, s33, s47
	v_sub_f32_e32 v13, v3, v1
	v_lshl_add_u64 v[112:113], v[4:5], 0, s[8:9]
	v_mul_lo_u32 v5, v16, 24
	v_or_b32_e32 v6, s0, v177
	v_sub_u32_e32 v30, v7, v5
	v_ashrrev_i32_e32 v7, 31, v6
	v_lshlrev_b64 v[114:115], 10, v[6:7]
	s_and_b32 s0, s0, 0x7f0
	s_cmp_eq_u32 s0, 0
	s_cselect_b64 s[44:45], -1, 0
	s_ashr_i32 s0, s33, 31
	s_lshr_b32 s0, s0, 21
	v_add_u32_e32 v108, 64, v104
	v_min_i32_e32 v15, 0x197, v108
	v_mul_hi_i32 v17, v15, s30
	s_and_b64 s[4:5], s[44:45], s[4:5]
	v_cndmask_b32_e64 v32, v16, 1, s[4:5]
	v_add_u32_e32 v35, 0x80, v104
	v_lshlrev_b32_e32 v20, 4, v104
	v_and_b32_e32 v10, 0xf0, v20
	s_movk_i32 s1, 0x290
	v_add_u32_e32 v21, s49, v10
	v_or_b32_e32 v10, s47, v177
	v_mad_u32_u24 v31, v10, s1, 0
	v_add_u32_e32 v22, 0x100, v104
	v_add_u32_e32 v23, 0x140, v104
	v_add_u32_e32 v24, 0x180, v104
	s_movk_i32 s6, 0x80
	v_cmp_gt_i32_e64 s[8:9], 64, v104
	v_ashrrev_i32_e32 v105, 31, v104
	s_movk_i32 s35, 0x190
	v_cndmask_b32_e64 v47, 0, v108, s[8:9]
	v_ashrrev_i32_e32 v182, 4, v47
	v_add_u32_e32 v25, 23, v104
	v_cmp_gt_u32_e64 s[18:19], 47, v25
	s_and_b64 s[80:81], s[18:19], s[44:45]
	v_writelane_b32 v254, s49, 23
	v_writelane_b32 v254, s47, 24
	s_add_i32 s33, s33, s47
	v_readlane_b32 s1, v254, 20
	s_waitcnt vmcnt(0)
	v_fmac_f32_e32 v1, v8, v13
	v_fmac_f32_e32 v11, v9, v14
	v_mul_f32_e32 v1, 0xbfb8aa3b, v1
	v_mul_f32_e32 v7, 0xbfb8aa3b, v11
	v_exp_f32_e32 v1, v1
	v_exp_f32_e32 v7, v7
	v_add_u32_e32 v8, s0, v6
	v_ashrrev_i32_e32 v28, 11, v8
	v_add_f32_e32 v1, 1.0, v1
	v_add_f32_e32 v7, 1.0, v7
	v_rcp_f32_e32 v1, v1
	v_rcp_f32_e32 v7, v7
	v_mul_i32_i24_e32 v8, 0x800, v28
	v_sub_u32_e32 v29, v6, v8
	v_ashrrev_i32_e32 v6, 2, v17
	v_cvt_pk_bf16_f32 v1, v1, v7
	ds_write_b32 v12, v1
	v_lshrrev_b32_e32 v1, 31, v17
	v_add_u32_e32 v1, v6, v1
	v_mul_lo_u32 v6, v1, 24
	v_sub_u32_e32 v33, v15, v6
	v_add_u32_e32 v6, 23, v15
	v_cmp_gt_u32_e64 s[4:5], 47, v6
	s_and_b64 s[4:5], s[44:45], s[4:5]
	s_movk_i32 s0, 0x198
	v_cndmask_b32_e64 v34, v1, 1, s[4:5]
	v_lshlrev_b32_e32 v1, 7, v33
	v_and_b32_e32 v6, 0xfffffc00, v1
	v_min_i32_e32 v1, 0x197, v35
	v_mul_hi_i32 v8, v1, s30
	v_lshrrev_b32_e32 v9, 31, v8
	v_ashrrev_i32_e32 v8, 2, v8
	v_add_u32_e32 v8, v8, v9
	v_mul_lo_u32 v9, v8, 24
	v_sub_u32_e32 v36, v1, v9
	v_add_u32_e32 v1, 23, v1
	v_cmp_gt_u32_e64 s[4:5], 47, v1
	s_and_b64 s[4:5], s[44:45], s[4:5]
	v_lshlrev_b32_e32 v1, 7, v36
	v_cndmask_b32_e64 v37, v8, 1, s[4:5]
	v_and_b32_e32 v8, 0xfffffc00, v1
	v_add_u32_e32 v1, 0xc0, v104
	v_min_i32_e32 v10, 0x197, v1
	v_mul_hi_i32 v11, v10, s30
	v_lshrrev_b32_e32 v12, 31, v11
	v_ashrrev_i32_e32 v11, 2, v11
	v_add_u32_e32 v11, v11, v12
	v_mul_lo_u32 v12, v11, 24
	v_sub_u32_e32 v38, v10, v12
	v_min_i32_e32 v12, 0x197, v22
	v_mul_hi_i32 v13, v12, s30
	v_lshrrev_b32_e32 v14, 31, v13
	v_ashrrev_i32_e32 v13, 2, v13
	v_add_u32_e32 v13, v13, v14
	v_mul_lo_u32 v14, v13, 24
	v_sub_u32_e32 v40, v12, v14
	v_min_i32_e32 v14, 0x197, v23
	v_mul_hi_i32 v15, v14, s30
	v_lshrrev_b32_e32 v16, 31, v15
	v_ashrrev_i32_e32 v15, 2, v15
	v_add_u32_e32 v15, v15, v16
	v_add_u32_e32 v10, 23, v10
	v_mul_lo_u32 v16, v15, 24
	v_cmp_gt_u32_e64 s[4:5], 47, v10
	v_sub_u32_e32 v42, v14, v16
	v_min_i32_e32 v16, 0x197, v24
	s_and_b64 s[4:5], s[44:45], s[4:5]
	v_add_u32_e32 v12, 23, v12
	v_mul_hi_i32 v17, v16, s30
	v_cndmask_b32_e64 v39, v11, 1, s[4:5]
	v_cmp_gt_u32_e64 s[4:5], 47, v12
	v_lshrrev_b32_e32 v18, 31, v17
	v_ashrrev_i32_e32 v17, 2, v17
	s_and_b64 s[4:5], s[44:45], s[4:5]
	v_add_u32_e32 v14, 23, v14
	v_add_u32_e32 v17, v17, v18
	v_cndmask_b32_e64 v41, v13, 1, s[4:5]
	v_cmp_gt_u32_e64 s[4:5], 47, v14
	v_mul_lo_u32 v18, v17, 24
	s_and_b64 s[4:5], s[44:45], s[4:5]
	v_sub_u32_e32 v44, v16, v18
	v_add_u32_e32 v16, 23, v16
	v_cndmask_b32_e64 v43, v15, 1, s[4:5]
	v_cmp_gt_u32_e64 s[4:5], 47, v16
	s_and_b64 s[4:5], s[44:45], s[4:5]
	v_cmp_gt_i32_e64 s[16:17], s0, v104
	v_cndmask_b32_e64 v45, v17, 1, s[4:5]
	v_cmp_gt_i32_e64 s[4:5], s6, v104
	s_movk_i32 s0, 0x158
	v_cmp_gt_i32_e64 s[18:19], s0, v104
	v_cndmask_b32_e64 v46, 0, v104, s[4:5]
	v_ashrrev_i32_e32 v181, 4, v46
	v_lshlrev_b32_e32 v18, 10, v181
	v_ashrrev_i32_e32 v19, 31, v18
	v_lshl_add_u64 v[116:117], v[18:19], 2, s[36:37]
	v_lshlrev_b32_e32 v18, 10, v182
	v_ashrrev_i32_e32 v19, 31, v18
	v_lshl_add_u64 v[118:119], v[18:19], 2, s[36:37]
	v_and_b32_e32 v18, v105, v35
	v_ashrrev_i32_e32 v183, 4, v18
	v_lshlrev_b32_e32 v18, 10, v183
	v_ashrrev_i32_e32 v19, 31, v18
	v_lshl_add_u64 v[120:121], v[18:19], 2, s[36:37]
	v_mul_hi_i32 v18, v104, s30
	v_lshrrev_b32_e32 v19, 31, v18
	v_ashrrev_i32_e32 v18, 2, v18
	v_add_u32_e32 v18, v18, v19
	v_mul_lo_u32 v19, v18, 24
	v_sub_u32_e32 v19, v104, v19
	v_lshlrev_b32_e32 v19, 4, v19
	v_mul_lo_u32 v18, v18, s35
	v_and_b32_e32 v25, 0xffffff80, v19
	v_add3_u32 v48, s49, v18, v25
	v_mul_hi_i32 v18, v108, s30
	v_and_b32_e32 v49, 0x70, v19
	v_lshrrev_b32_e32 v19, 31, v18
	v_ashrrev_i32_e32 v18, 2, v18
	v_add_u32_e32 v18, v18, v19
	v_mul_lo_u32 v19, v18, 24
	v_sub_u32_e32 v19, v108, v19
	v_add_u32_e32 v25, 0x57, v104
	v_lshlrev_b32_e32 v19, 4, v19
	v_cmp_gt_u32_e64 s[20:21], 47, v25
	v_mul_lo_u32 v18, v18, s35
	v_and_b32_e32 v25, 0xffffff80, v19
	v_add3_u32 v50, s49, v18, v25
	v_mul_hi_i32 v18, v35, s30
	v_and_b32_e32 v51, 0x70, v19
	v_lshrrev_b32_e32 v19, 31, v18
	v_ashrrev_i32_e32 v18, 2, v18
	v_add_u32_e32 v18, v18, v19
	v_mul_lo_u32 v19, v18, 24
	v_sub_u32_e32 v19, v35, v19
	v_add_u32_e32 v25, 0x97, v104
	v_lshlrev_b32_e32 v19, 4, v19
	v_cmp_gt_u32_e64 s[22:23], 47, v25
	v_mul_lo_u32 v18, v18, s35
	v_and_b32_e32 v25, 0xffffff80, v19
	v_add3_u32 v52, s49, v18, v25
	v_mul_hi_i32 v18, v1, s30
	v_and_b32_e32 v53, 0x70, v19
	v_lshrrev_b32_e32 v19, 31, v18
	v_ashrrev_i32_e32 v18, 2, v18
	v_add_u32_e32 v18, v18, v19
	v_mul_lo_u32 v19, v18, 24
	v_sub_u32_e32 v1, v1, v19
	v_add_u32_e32 v19, 0xd7, v104
	v_lshlrev_b32_e32 v1, 4, v1
	v_cmp_gt_u32_e64 s[24:25], 47, v19
	v_mul_lo_u32 v18, v18, s35
	v_and_b32_e32 v19, 0xffffff80, v1
	v_and_b32_e32 v55, 0x70, v1
	v_mul_hi_i32 v1, v22, s30
	v_add3_u32 v54, s49, v18, v19
	v_lshrrev_b32_e32 v18, 31, v1
	v_ashrrev_i32_e32 v1, 2, v1
	v_add_u32_e32 v1, v1, v18
	v_mul_lo_u32 v18, v1, 24
	v_sub_u32_e32 v18, v22, v18
	v_add_u32_e32 v19, 0x117, v104
	v_lshlrev_b32_e32 v18, 4, v18
	v_cmp_gt_u32_e64 s[26:27], 47, v19
	v_mul_lo_u32 v1, v1, s35
	v_and_b32_e32 v19, 0xffffff80, v18
	v_add3_u32 v56, s49, v1, v19
	v_mul_hi_i32 v1, v23, s30
	v_and_b32_e32 v57, 0x70, v18
	v_lshrrev_b32_e32 v18, 31, v1
	v_ashrrev_i32_e32 v1, 2, v1
	v_add_u32_e32 v1, v1, v18
	v_mul_lo_u32 v18, v1, 24
	v_sub_u32_e32 v18, v23, v18
	v_add_u32_e32 v19, 0x157, v104
	v_lshlrev_b32_e32 v18, 4, v18
	v_cmp_gt_u32_e64 s[28:29], 47, v19
	v_mul_lo_u32 v1, v1, s35
	v_and_b32_e32 v19, 0xffffff80, v18
	v_add3_u32 v58, s49, v1, v19
	v_mul_hi_i32 v1, v24, s30
	s_movk_i32 s0, 0x118
	v_and_b32_e32 v59, 0x70, v18
	v_lshrrev_b32_e32 v18, 31, v1
	v_ashrrev_i32_e32 v1, 2, v1
	s_and_b64 s[82:83], s[20:21], s[44:45]
	v_cmp_gt_i32_e64 s[20:21], s0, v104
	s_movk_i32 s0, 0xd8
	v_add_u32_e32 v1, v1, v18
	s_and_b64 s[84:85], s[22:23], s[44:45]
	v_cmp_gt_i32_e64 s[22:23], s0, v104
	s_movk_i32 s0, 0x98
	v_mul_lo_u32 v18, v1, 24
	s_and_b64 s[86:87], s[24:25], s[44:45]
	v_cmp_gt_i32_e64 s[24:25], s0, v104
	s_movk_i32 s0, 0x58
	v_sub_u32_e32 v18, v24, v18
	v_add_u32_e32 v19, 0x197, v104
	s_and_b64 s[88:89], s[26:27], s[44:45]
	v_cmp_gt_i32_e64 s[26:27], s0, v104
	v_cmp_gt_u32_e64 s[30:31], 47, v19
	v_lshlrev_b32_e32 v18, 4, v18
	v_add_u32_e32 v24, 16, v2
	s_lshr_b32 s0, s1, 3
	s_and_b64 s[90:91], s[28:29], s[44:45]
	s_and_b64 s[92:93], s[30:31], s[44:45]
	v_mul_lo_u32 v1, v1, s35
	v_and_b32_e32 v19, 0xffffff80, v18
	v_and_b32_e32 v61, 0x70, v18
	v_lshlrev_b32_e32 v18, 2, v24
	v_add_u32_e32 v25, 32, v2
	v_lshlrev_b32_e32 v62, 1, v24
	v_add_u32_e32 v24, s33, v177
	s_and_b32 s0, s0, 0x1ffffff0
	v_add3_u32 v60, s49, v1, v19
	v_and_b32_e32 v1, 0xffffff00, v20
	v_lshlrev_b32_e32 v20, 2, v25
	v_add_u32_e32 v26, 48, v2
	v_lshlrev_b32_e32 v63, 1, v25
	v_ashrrev_i32_e32 v25, 31, v24
	s_add_u32 s30, s60, s0
	v_lshlrev_b32_e32 v22, 2, v26
	v_lshlrev_b32_e32 v64, 1, v26
	v_lshlrev_b64 v[26:27], 6, v[24:25]
	v_writelane_b32 v254, s0, 25
	s_addc_u32 s31, s61, 0
	s_lshl_b32 s0, s1, 1
	v_add_u32_e32 v184, v21, v1
	v_lshlrev_b32_e32 v1, 4, v108
	v_lshl_add_u64 v[26:27], s[30:31], 0, v[26:27]
	s_mov_b64 s[30:31], 0x4c0000
	s_and_b32 s64, s0, 0xffffff00
	s_movk_i32 s0, 0x300
	v_and_b32_e32 v1, 0xffffff00, v1
	v_lshl_add_u64 v[122:123], v[26:27], 0, s[30:31]
	v_lshl_add_u32 v28, v28, 4, s46
	v_mad_i64_i32 v[26:27], s[30:31], v29, s0, 0
	s_mov_b32 s0, 0x180000
	v_add_u32_e32 v185, v21, v1
	v_lshlrev_b32_e32 v1, 4, v35
	v_mad_i64_i32 v[26:27], s[30:31], v28, s0, v[26:27]
	v_and_b32_e32 v0, -16, v104
	v_and_b32_e32 v1, 0xffffff00, v1
	v_lshl_add_u64 v[28:29], v[26:27], 0, v[110:111]
	v_add_u32_e32 v186, v21, v1
	v_ashrrev_i32_e32 v1, 31, v0
	v_lshl_add_u64 v[28:29], s[60:61], 0, v[28:29]
	s_mov_b64 s[30:31], 0x3e480140
	v_ashrrev_i32_e32 v3, 31, v2
	v_ashrrev_i32_e32 v19, 31, v18
	v_lshl_add_u64 v[124:125], v[28:29], 0, s[30:31]
	v_lshl_add_u64 v[28:29], v[26:27], 0, v[0:1]
	v_add_u32_e32 v111, s64, v2
	v_lshl_add_u64 v[28:29], s[60:61], 0, v[28:29]
	s_mov_b64 s[36:37], 0x3e480000
	v_lshl_add_u64 v[18:19], v[26:27], 0, v[18:19]
	v_lshlrev_b64 v[2:3], 1, v[2:3]
	v_lshl_add_u64 v[126:127], v[28:29], 0, s[36:37]
	v_sub_co_u32_e64 v28, s[30:31], v18, v2
	v_ashrrev_i32_e32 v21, 31, v20
	s_nop 0
	v_subb_co_u32_e64 v29, s[30:31], v19, v3, s[30:31]
	v_lshl_add_u64 v[18:19], s[60:61], 0, v[18:19]
	v_lshl_add_u64 v[130:131], v[18:19], 0, s[36:37]
	v_lshl_add_u64 v[18:19], v[26:27], 0, v[20:21]
	v_sub_co_u32_e64 v20, s[30:31], v18, v2
	v_ashrrev_i32_e32 v23, 31, v22
	s_nop 0
	v_subb_co_u32_e64 v21, s[30:31], v19, v3, s[30:31]
	v_lshl_add_u64 v[18:19], s[60:61], 0, v[18:19]
	v_lshl_add_u64 v[134:135], v[18:19], 0, s[36:37]
	v_lshl_add_u64 v[18:19], v[26:27], 0, v[22:23]
	v_mov_b32_e32 v4, s49
	v_lshl_add_u64 v[132:133], s[60:61], 0, v[20:21]
	v_sub_co_u32_e64 v20, s[30:31], v18, v2
	s_mov_b32 s65, 0
	v_mad_u32_u24 v180, v177, s35, v4
	v_lshlrev_b32_e32 v4, 7, v30
	v_subb_co_u32_e64 v21, s[30:31], v19, v3, s[30:31]
	v_lshl_add_u64 v[18:19], s[60:61], 0, v[18:19]
	v_add3_u32 v1, s33, v32, -1
	s_movk_i32 s0, 0x3400
	v_and_b32_e32 v4, 0xfffffc00, v4
	v_lshl_add_u64 v[138:139], v[18:19], 0, s[36:37]
	v_mad_i64_i32 v[18:19], s[30:31], v1, s0, 0
	v_and_b32_e32 v1, 7, v30
	s_lshl_b64 s[36:37], s[64:65], 1
	v_ashrrev_i32_e32 v5, 31, v4
	v_writelane_b32 v254, s46, 26
	v_lshl_or_b32 v18, v1, 4, v18
	s_add_u32 s30, s60, s36
	v_lshl_add_u64 v[4:5], v[4:5], 1, v[18:19]
	v_writelane_b32 v254, s36, 27
	s_addc_u32 s31, s61, s37
	v_lshl_add_u64 v[4:5], s[30:31], 0, v[4:5]
	v_writelane_b32 v254, s37, 28
	s_mov_b64 s[36:37], 0x37c80000
	v_add3_u32 v1, s33, v34, -1
	v_lshl_add_u64 v[140:141], v[4:5], 0, s[36:37]
	v_mad_i64_i32 v[4:5], s[44:45], v1, s0, 0
	v_and_b32_e32 v1, 7, v33
	v_ashrrev_i32_e32 v7, 31, v6
	v_lshl_or_b32 v4, v1, 4, v4
	v_lshl_add_u64 v[4:5], v[6:7], 1, v[4:5]
	v_lshl_add_u64 v[4:5], s[30:31], 0, v[4:5]
	v_add3_u32 v1, s33, v37, -1
	v_lshl_add_u64 v[142:143], v[4:5], 0, s[36:37]
	v_mad_i64_i32 v[4:5], s[44:45], v1, s0, 0
	v_and_b32_e32 v1, 7, v36
	v_ashrrev_i32_e32 v9, 31, v8
	v_lshl_or_b32 v4, v1, 4, v4
	v_lshl_add_u64 v[4:5], v[8:9], 1, v[4:5]
	v_lshlrev_b32_e32 v10, 7, v38
	v_lshl_add_u64 v[4:5], s[30:31], 0, v[4:5]
	v_add3_u32 v1, s33, v39, -1
	v_and_b32_e32 v10, 0xfffffc00, v10
	v_lshl_add_u64 v[144:145], v[4:5], 0, s[36:37]
	v_mad_i64_i32 v[4:5], s[44:45], v1, s0, 0
	v_and_b32_e32 v1, 7, v38
	v_ashrrev_i32_e32 v11, 31, v10
	v_lshl_or_b32 v4, v1, 4, v4
	v_lshl_add_u64 v[4:5], v[10:11], 1, v[4:5]
	v_lshlrev_b32_e32 v12, 7, v40
	v_lshl_add_u64 v[4:5], s[30:31], 0, v[4:5]
	v_add3_u32 v1, s33, v41, -1
	v_and_b32_e32 v12, 0xfffffc00, v12
	v_lshl_add_u64 v[146:147], v[4:5], 0, s[36:37]
	v_mad_i64_i32 v[4:5], s[44:45], v1, s0, 0
	v_and_b32_e32 v1, 7, v40
	v_ashrrev_i32_e32 v13, 31, v12
	v_lshl_or_b32 v4, v1, 4, v4
	v_lshl_add_u64 v[4:5], v[12:13], 1, v[4:5]
	v_lshlrev_b32_e32 v14, 7, v42
	v_lshl_add_u64 v[4:5], s[30:31], 0, v[4:5]
	v_add3_u32 v1, s33, v43, -1
	v_and_b32_e32 v14, 0xfffffc00, v14
	v_lshl_add_u64 v[150:151], v[4:5], 0, s[36:37]
	v_mad_i64_i32 v[4:5], s[44:45], v1, s0, 0
	v_and_b32_e32 v1, 7, v42
	v_ashrrev_i32_e32 v15, 31, v14
	v_lshl_or_b32 v4, v1, 4, v4
	v_lshl_add_u64 v[4:5], v[14:15], 1, v[4:5]
	v_lshlrev_b32_e32 v16, 7, v44
	v_lshl_add_u64 v[4:5], s[30:31], 0, v[4:5]
	v_add3_u32 v1, s33, v45, -1
	v_and_b32_e32 v16, 0xfffffc00, v16
	v_lshl_add_u64 v[152:153], v[4:5], 0, s[36:37]
	v_mad_i64_i32 v[4:5], s[44:45], v1, s0, 0
	v_and_b32_e32 v1, 7, v44
	v_ashrrev_i32_e32 v17, 31, v16
	v_lshl_or_b32 v4, v1, 4, v4
	v_lshl_add_u64 v[4:5], v[16:17], 1, v[4:5]
	v_lshl_add_u64 v[4:5], s[30:31], 0, v[4:5]
	v_lshl_add_u64 v[154:155], v[4:5], 0, s[36:37]
	v_and_b32_e32 v1, 15, v46
	s_lshl_b64 s[0:1], s[64:65], 2
	v_lshlrev_b64 v[4:5], 11, v[24:25]
	v_lshl_or_b32 v156, v1, 4, s0
	v_and_b32_e32 v1, 15, v47
	v_lshl_add_u64 v[2:3], v[4:5], 0, v[2:3]
	v_mov_b32_e32 v157, s1
	v_lshl_or_b32 v158, v1, 4, s0
	v_bitop3_b32 v1, v105, 15, v35 bitop3:0x80
	v_lshl_add_u64 v[2:3], s[30:31], 0, v[2:3]
	s_mov_b64 s[30:31], 0x4a480040
	v_cmp_gt_u32_e32 vcc, 16, v104
	v_add_u32_e32 v179, s49, v0
	v_cmp_lt_i32_e64 s[6:7], 2, v181
	v_cmp_lt_i32_e64 s[10:11], 2, v182
	v_cmp_gt_i32_e64 s[12:13], 0, v104
	v_cmp_lt_i32_e64 s[14:15], 2, v183
	v_cmp_gt_i32_e64 s[28:29], 24, v104
	v_or_b32_e32 v187, s64, v177
	v_lshl_add_u64 v[128:129], s[60:61], 0, v[28:29]
	v_lshl_add_u64 v[136:137], s[60:61], 0, v[20:21]
	v_mov_b32_e32 v159, s1
	v_writelane_b32 v254, s0, 29
	v_mov_b32_e32 v165, v157
	v_lshl_add_u64 v[166:167], v[2:3], 0, s[30:31]
	v_lshl_or_b32 v164, v1, 4, s0
	s_movk_i32 s33, 0x280
	v_add_u32_e32 v188, v48, v49
	v_add_u32_e32 v189, v50, v51
	v_add_u32_e32 v190, v52, v53
	v_add_u32_e32 v191, v54, v55
	v_add_u32_e32 v192, v56, v57
	v_add_u32_e32 v193, v58, v59
	v_add_u32_e32 v194, v60, v61
	s_mov_b32 s35, 0xc1a00000
	s_mov_b32 s50, 0x800000
	s_mov_b32 s51, 0x3f317217
	s_mov_b32 s52, 0x7f800000
	s_mov_b32 s53, 0x3e480000
	s_mov_b64 s[94:95], 0x180000
	s_mov_b64 s[96:97], 0x80
	s_mov_b64 s[44:45], 0x100
	v_add_u32_e32 v195, v31, v0
	v_mov_b32_e32 v196, 0x41b17218
	v_add_u32_e32 v197, v180, v62
	v_add_u32_e32 v198, v180, v63
	v_add_u32_e32 v199, v180, v64
	s_waitcnt lgkmcnt(0)
	s_barrier
	v_writelane_b32 v254, s1, 30
	s_branch .LBB0_289

.LBB0_1361:
	s_or_b64 exec, exec, s[4:5]
	s_waitcnt lgkmcnt(0)
	v_mov_b32_e32 v0, s2
	v_readlane_b32 s0, v254, 0
	s_barrier
	v_mbcnt_lo_u32_b32 v104, -1, 0
	v_mbcnt_hi_u32_b32 v104, -1, v104
	s_movk_i32 s4, 0x3400
	v_add_u32_e32 v106, s0, v104
	v_readlane_b32 s0, v254, 18
	v_readfirstlane_b32 s78, v0
	v_mov_b32_e32 v0, 0
	v_readlane_b32 s1, v254, 19
	s_load_dwordx2 s[80:81], s[0:1], 0x188
	s_load_dwordx4 s[40:43], s[0:1], 0xd8
	v_readfirstlane_b32 s82, v0
	s_ashr_i32 s83, s82, 31
	v_ashrrev_i32_e32 v105, 4, v106
	s_waitcnt lgkmcnt(0)
	s_add_u32 s74, s80, s82
	s_addc_u32 s75, s81, s83
	s_add_u32 s0, s74, 0x37c80000
	s_addc_u32 s1, s75, 0
	s_lshl_b32 s33, s78, 5
	v_add_u32_e32 v9, s33, v105
	v_mov_b64_e32 v[0:1], s[0:1]
	v_mad_i64_i32 v[0:1], s[4:5], v9, s4, v[0:1]
	v_lshlrev_b32_e32 v176, 1, v104
	s_mov_b64 s[4:5], 0x1800
	v_and_b32_e32 v10, 30, v176
	v_mov_b32_e32 v5, 0
	v_lshl_add_u64 v[2:3], v[0:1], 0, s[4:5]
	v_lshlrev_b32_e32 v4, 1, v10
	v_lshl_add_u64 v[6:7], v[2:3], 0, v[4:5]
	global_load_dword v8, v[6:7], off
	global_load_dword v202, v[6:7], off offset:128
	global_load_dword v203, v[6:7], off offset:192
	global_load_dword v204, v[6:7], off offset:256
	global_load_dword v205, v[6:7], off offset:320
	global_load_dword v206, v[6:7], off offset:384
	global_load_dword v207, v[6:7], off offset:448
	global_load_dword v208, v[6:7], off offset:512
	global_load_dword v209, v[6:7], off offset:576
	s_movk_i32 s4, 0xe400
	v_and_b32_e32 v6, 0x7ff, v9
	s_mov_b32 s5, -1
	v_cmp_ne_u32_e32 vcc, 0, v6
	v_lshl_add_u64 v[0:1], v[0:1], 0, s[4:5]
	v_mov_b32_e32 v9, 0
	s_and_saveexec_b64 s[4:5], vcc
	s_cbranch_execz .LBB0_1363
	v_mov_b32_e32 v7, 0
	v_mov_b32_e32 v6, v4
	v_lshl_add_u64 v[6:7], v[0:1], 0, v[6:7]
	global_load_dword v9, v[6:7], off
	global_load_dword v211, v[6:7], off offset:64
	global_load_dword v212, v[6:7], off offset:128
	global_load_dword v213, v[6:7], off offset:192
	global_load_dword v214, v[6:7], off offset:256
	global_load_dword v215, v[6:7], off offset:320
	global_load_dword v216, v[6:7], off offset:384
	global_load_dword v217, v[6:7], off offset:448
	global_load_dword v218, v[6:7], off offset:512
	global_load_dword v219, v[6:7], off offset:576
.LBB0_1363:
	s_or_b64 exec, exec, s[4:5]
	s_add_u32 s6, s40, 0x3000
	s_addc_u32 s7, s41, 0
	v_lshlrev_b32_e32 v4, 2, v10
	global_load_dwordx2 v[12:13], v4, s[6:7]
	global_load_dwordx2 v[222:223], v4, s[6:7] offset:128
	global_load_dwordx2 v[224:225], v4, s[6:7] offset:256
	global_load_dwordx2 v[226:227], v4, s[6:7] offset:384
	global_load_dwordx2 v[228:229], v4, s[6:7] offset:512
	global_load_dwordx2 v[230:231], v4, s[6:7] offset:640
	global_load_dwordx2 v[232:233], v4, s[6:7] offset:768
	global_load_dwordx2 v[234:235], v4, s[6:7] offset:896
	global_load_dwordx2 v[236:237], v4, s[6:7] offset:1024
	global_load_dwordx2 v[238:239], v4, s[6:7] offset:1152
	v_or_b32_e32 v6, 32, v10
	v_lshlrev_b32_e32 v4, 1, v6
	v_lshl_add_u64 v[14:15], v[2:3], 0, v[4:5]
	global_load_dword v7, v[14:15], off
	s_waitcnt vmcnt(0)
	v_and_b32_e32 v11, 0xffff0000, v8
	v_and_b32_e32 v14, 0xffff0000, v9
	v_lshlrev_b32_e32 v8, 16, v8
	v_lshlrev_b32_e32 v9, 16, v9
	v_sub_f32_e32 v14, v14, v11
	v_sub_f32_e32 v9, v9, v8
	v_readlane_b32 s8, v254, 18
	v_readlane_b32 s9, v254, 19
	s_load_dwordx2 s[4:5], s[8:9], 0x128
	s_load_dwordx4 s[44:47], s[8:9], 0x118
	s_load_dwordx2 s[84:85], s[8:9], 0xf0
	s_load_dwordx2 s[12:13], s[8:9], 0x108
	s_movk_i32 s8, 0x290
	s_waitcnt vmcnt(1)
	v_fmac_f32_e32 v11, v13, v14
	v_fmac_f32_e32 v8, v12, v9
	v_add_f32_e32 v9, v11, v11
	v_add_f32_e32 v8, v8, v8
	v_mul_f32_e32 v9, 0x3fb8aa3b, v9
	v_mul_f32_e32 v8, 0x3fb8aa3b, v8
	v_exp_f32_e32 v9, v9
	v_exp_f32_e32 v8, v8
	v_mul_lo_u32 v11, v105, s8
	v_add_u32_e32 v11, 0, v11
	v_add_f32_e32 v9, 1.0, v9
	v_add_f32_e32 v8, 1.0, v8
	v_rcp_f32_e32 v9, v9
	v_rcp_f32_e32 v8, v8
	s_nop 0
	v_pk_fma_f32 v[8:9], v[8:9], -2.0, 1.0 op_sel_hi:[1,0,0]
	s_nop 0
	v_cvt_pk_bf16_f32 v8, v8, v9
	v_lshl_add_u32 v9, v10, 1, v11
	ds_write_b32 v9, v8
	s_and_saveexec_b64 s[8:9], vcc
	s_cbranch_execz .LBB0_1365
	v_mov_b32_e32 v5, 0
	v_lshl_add_u64 v[4:5], v[0:1], 0, v[4:5]
	v_mov_b32_e32 v5, v211
.LBB0_1365:
	s_or_b64 exec, exec, s[8:9]
	v_lshlrev_b32_e32 v4, 2, v6
	v_mov_b64_e32 v[14:15], v[222:223]
	v_or_b32_e32 v4, 64, v10
	v_mov_b32_e32 v9, 0
	v_lshlrev_b32_e32 v8, 1, v4
	v_lshl_add_u64 v[12:13], v[2:3], 0, v[8:9]
	v_mov_b32_e32 v12, v202
	s_waitcnt vmcnt(2)
	v_and_b32_e32 v13, 0xffff0000, v7
	v_and_b32_e32 v16, 0xffff0000, v5
	v_lshlrev_b32_e32 v7, 16, v7
	v_lshlrev_b32_e32 v5, 16, v5
	v_sub_f32_e32 v16, v16, v13
	v_sub_f32_e32 v5, v5, v7
	s_waitcnt vmcnt(1)
	v_fmac_f32_e32 v13, v15, v16
	v_fmac_f32_e32 v7, v14, v5
	v_add_f32_e32 v5, v13, v13
	v_add_f32_e32 v7, v7, v7
	v_mul_f32_e32 v5, 0x3fb8aa3b, v5
	v_mul_f32_e32 v7, 0x3fb8aa3b, v7
	v_exp_f32_e32 v5, v5
	v_exp_f32_e32 v7, v7
	v_add_f32_e32 v5, 1.0, v5
	v_add_f32_e32 v7, 1.0, v7
	v_rcp_f32_e32 v15, v5
	v_rcp_f32_e32 v14, v7
	v_lshl_add_u32 v5, v6, 1, v11
	v_pk_fma_f32 v[6:7], v[14:15], -2.0, 1.0 op_sel_hi:[1,0,0]
	s_nop 0
	v_cvt_pk_bf16_f32 v6, v6, v7
	ds_write_b32 v5, v6
	v_mov_b32_e32 v5, 0
	s_and_saveexec_b64 s[8:9], vcc
	s_cbranch_execz .LBB0_1367
	v_mov_b32_e32 v7, 0
	v_mov_b32_e32 v6, v8
	v_lshl_add_u64 v[6:7], v[0:1], 0, v[6:7]
	v_mov_b32_e32 v5, v212
.LBB0_1367:
	s_or_b64 exec, exec, s[8:9]
	v_lshlrev_b32_e32 v6, 2, v4
	v_or_b32_e32 v13, 0x60, v10
	v_mov_b64_e32 v[6:7], v[224:225]
	v_lshlrev_b32_e32 v8, 1, v13
	v_lshl_add_u64 v[14:15], v[2:3], 0, v[8:9]
	v_mov_b32_e32 v14, v203
	s_waitcnt vmcnt(2)
	v_lshlrev_b32_e32 v16, 16, v12
	v_lshlrev_b32_e32 v18, 16, v5
	v_and_b32_e32 v17, 0xffff0000, v12
	v_and_b32_e32 v19, 0xffff0000, v5
	v_pk_add_f32 v[18:19], v[18:19], v[16:17] neg_lo:[0,1] neg_hi:[0,1]
	v_lshl_add_u32 v4, v4, 1, v11
	s_waitcnt vmcnt(1)
	v_pk_fma_f32 v[6:7], v[6:7], v[18:19], v[16:17]
	s_nop 0
	v_cvt_pk_bf16_f32 v5, v6, v7
	ds_write_b32 v4, v5
	s_and_saveexec_b64 s[8:9], vcc
	s_cbranch_execz .LBB0_1369
	v_mov_b32_e32 v9, 0
	v_lshl_add_u64 v[4:5], v[0:1], 0, v[8:9]
	v_mov_b32_e32 v9, v213
.LBB0_1369:
	s_or_b64 exec, exec, s[8:9]
	v_lshlrev_b32_e32 v4, 2, v13
	v_mov_b64_e32 v[16:17], v[226:227]
	v_or_b32_e32 v4, 0x80, v10
	v_mov_b32_e32 v7, 0
	v_lshlrev_b32_e32 v6, 1, v4
	v_lshl_add_u64 v[18:19], v[2:3], 0, v[6:7]
	v_mov_b32_e32 v5, v204
	s_waitcnt vmcnt(2)
	v_lshlrev_b32_e32 v18, 16, v14
	v_lshlrev_b32_e32 v8, 16, v9
	v_and_b32_e32 v19, 0xffff0000, v14
	v_and_b32_e32 v9, 0xffff0000, v9
	v_pk_add_f32 v[8:9], v[8:9], v[18:19] neg_lo:[0,1] neg_hi:[0,1]
	v_lshl_add_u32 v12, v13, 1, v11
	s_waitcnt vmcnt(1)
	v_pk_fma_f32 v[8:9], v[16:17], v[8:9], v[18:19]
	s_nop 0
	v_cvt_pk_bf16_f32 v8, v8, v9
	ds_write_b32 v12, v8
	v_mov_b32_e32 v12, 0
	s_and_saveexec_b64 s[8:9], vcc
	s_cbranch_execz .LBB0_1371
	v_mov_b32_e32 v9, 0
	v_mov_b32_e32 v8, v6
	v_lshl_add_u64 v[8:9], v[0:1], 0, v[8:9]
	v_mov_b32_e32 v12, v214
.LBB0_1371:
	s_or_b64 exec, exec, s[8:9]
	v_lshlrev_b32_e32 v6, 2, v4
	v_mov_b64_e32 v[14:15], v[228:229]
	v_or_b32_e32 v8, 0xa0, v10
	v_lshlrev_b32_e32 v6, 1, v8
	v_lshl_add_u64 v[16:17], v[2:3], 0, v[6:7]
	v_mov_b32_e32 v9, v205
	s_waitcnt vmcnt(2)
	v_lshlrev_b32_e32 v13, 16, v5
	v_lshlrev_b32_e32 v16, 16, v12
	v_and_b32_e32 v5, 0xffff0000, v5
	v_and_b32_e32 v12, 0xffff0000, v12
	v_sub_f32_e32 v16, v16, v13
	v_sub_f32_e32 v12, v12, v5
	v_lshl_add_u32 v4, v4, 1, v11
	s_waitcnt vmcnt(1)
	v_fmac_f32_e32 v13, v14, v16
	v_fmac_f32_e32 v5, v15, v12
	v_mul_f32_e32 v5, 0xbfb8aa3b, v5
	v_mul_f32_e32 v12, 0xbfb8aa3b, v13
	v_exp_f32_e32 v5, v5
	v_exp_f32_e32 v12, v12
	v_add_f32_e32 v5, 1.0, v5
	v_add_f32_e32 v12, 1.0, v12
	v_rcp_f32_e32 v5, v5
	v_rcp_f32_e32 v12, v12
	s_nop 0
	v_cvt_pk_bf16_f32 v5, v12, v5
	ds_write_b32 v4, v5
	s_and_saveexec_b64 s[8:9], vcc
	s_cbranch_execz .LBB0_1373
	v_mov_b32_e32 v7, 0
	v_lshl_add_u64 v[4:5], v[0:1], 0, v[6:7]
	v_mov_b32_e32 v7, v215
.LBB0_1373:
	s_or_b64 exec, exec, s[8:9]
	v_lshlrev_b32_e32 v4, 2, v8
	v_mov_b64_e32 v[14:15], v[230:231]
	v_or_b32_e32 v6, 0xc0, v10
	v_mov_b32_e32 v5, 0
	v_lshlrev_b32_e32 v4, 1, v6
	v_lshl_add_u64 v[12:13], v[2:3], 0, v[4:5]
	v_mov_b32_e32 v12, v206
	s_waitcnt vmcnt(2)
	v_lshlrev_b32_e32 v13, 16, v9
	v_lshlrev_b32_e32 v16, 16, v7
	v_and_b32_e32 v9, 0xffff0000, v9
	v_and_b32_e32 v7, 0xffff0000, v7
	v_sub_f32_e32 v16, v16, v13
	v_sub_f32_e32 v7, v7, v9
	v_lshl_add_u32 v8, v8, 1, v11
	s_waitcnt vmcnt(1)
	v_fmac_f32_e32 v13, v14, v16
	v_fmac_f32_e32 v9, v15, v7
	v_mul_f32_e32 v7, 0xbfb8aa3b, v9
	v_mul_f32_e32 v9, 0xbfb8aa3b, v13
	v_exp_f32_e32 v7, v7
	v_exp_f32_e32 v9, v9
	v_add_f32_e32 v7, 1.0, v7
	v_add_f32_e32 v9, 1.0, v9
	v_rcp_f32_e32 v7, v7
	v_rcp_f32_e32 v9, v9
	s_nop 0
	v_cvt_pk_bf16_f32 v7, v9, v7
	ds_write_b32 v8, v7
	v_mov_b32_e32 v7, 0
	s_and_saveexec_b64 s[8:9], vcc
	s_cbranch_execz .LBB0_1375
	v_mov_b32_e32 v9, 0
	v_mov_b32_e32 v8, v4
	v_lshl_add_u64 v[8:9], v[0:1], 0, v[8:9]
	v_mov_b32_e32 v7, v216
.LBB0_1375:
	s_or_b64 exec, exec, s[8:9]
	v_lshlrev_b32_e32 v4, 2, v6
	v_mov_b64_e32 v[14:15], v[232:233]
	v_or_b32_e32 v8, 0xe0, v10
	v_lshlrev_b32_e32 v4, 1, v8
	v_lshl_add_u64 v[16:17], v[2:3], 0, v[4:5]
	v_mov_b32_e32 v9, v207
	s_waitcnt vmcnt(2)
	v_lshlrev_b32_e32 v13, 16, v12
	v_lshlrev_b32_e32 v16, 16, v7
	v_and_b32_e32 v12, 0xffff0000, v12
	v_and_b32_e32 v7, 0xffff0000, v7
	v_sub_f32_e32 v16, v16, v13
	v_sub_f32_e32 v7, v7, v12
	v_lshl_add_u32 v6, v6, 1, v11
	s_waitcnt vmcnt(1)
	v_fmac_f32_e32 v13, v14, v16
	v_fmac_f32_e32 v12, v15, v7
	v_mul_f32_e32 v7, 0xbfb8aa3b, v12
	v_mul_f32_e32 v12, 0xbfb8aa3b, v13
	v_exp_f32_e32 v7, v7
	v_exp_f32_e32 v12, v12
	v_add_f32_e32 v7, 1.0, v7
	v_add_f32_e32 v12, 1.0, v12
	v_rcp_f32_e32 v7, v7
	v_rcp_f32_e32 v12, v12
	s_nop 0
	v_cvt_pk_bf16_f32 v7, v12, v7
	ds_write_b32 v6, v7
	s_and_saveexec_b64 s[8:9], vcc
	s_cbranch_execz .LBB0_1377
	v_mov_b32_e32 v5, 0
	v_lshl_add_u64 v[4:5], v[0:1], 0, v[4:5]
	v_mov_b32_e32 v5, v217
.LBB0_1377:
	s_or_b64 exec, exec, s[8:9]
	v_lshlrev_b32_e32 v4, 2, v8
	v_mov_b64_e32 v[14:15], v[234:235]
	v_or_b32_e32 v4, 0x100, v10
	v_mov_b32_e32 v7, 0
	v_lshlrev_b32_e32 v6, 1, v4
	v_lshl_add_u64 v[12:13], v[2:3], 0, v[6:7]
	v_mov_b32_e32 v12, v208
	s_waitcnt vmcnt(2)
	v_lshlrev_b32_e32 v13, 16, v9
	v_lshlrev_b32_e32 v16, 16, v5
	v_and_b32_e32 v9, 0xffff0000, v9
	v_and_b32_e32 v5, 0xffff0000, v5
	v_sub_f32_e32 v16, v16, v13
	v_sub_f32_e32 v5, v5, v9
	v_lshl_add_u32 v8, v8, 1, v11
	s_waitcnt vmcnt(1)
	v_fmac_f32_e32 v13, v14, v16
	v_fmac_f32_e32 v9, v15, v5
	v_mul_f32_e32 v5, 0xbfb8aa3b, v9
	v_mul_f32_e32 v9, 0xbfb8aa3b, v13
	v_exp_f32_e32 v5, v5
	v_exp_f32_e32 v9, v9
	v_add_f32_e32 v5, 1.0, v5
	v_add_f32_e32 v9, 1.0, v9
	v_rcp_f32_e32 v5, v5
	v_rcp_f32_e32 v9, v9
	s_nop 0
	v_cvt_pk_bf16_f32 v5, v9, v5
	ds_write_b32 v8, v5
	v_mov_b32_e32 v8, 0
	s_and_saveexec_b64 s[8:9], vcc
	s_cbranch_execz .LBB0_1379
	v_mov_b32_e32 v9, 0
	v_mov_b32_e32 v8, v6
	v_lshl_add_u64 v[8:9], v[0:1], 0, v[8:9]
	v_mov_b32_e32 v8, v218
.LBB0_1379:
	s_or_b64 exec, exec, s[8:9]
	v_lshlrev_b32_e32 v5, 2, v4
	v_mov_b64_e32 v[14:15], v[236:237]
	v_or_b32_e32 v5, 0x120, v10
	v_lshlrev_b32_e32 v6, 1, v5
	v_lshl_add_u64 v[2:3], v[2:3], 0, v[6:7]
	v_mov_b32_e32 v2, v209
	s_waitcnt vmcnt(2)
	v_lshlrev_b32_e32 v3, 16, v12
	v_lshlrev_b32_e32 v9, 16, v8
	v_and_b32_e32 v10, 0xffff0000, v12
	v_and_b32_e32 v8, 0xffff0000, v8
	v_sub_f32_e32 v9, v9, v3
	v_sub_f32_e32 v8, v8, v10
	v_lshl_add_u32 v4, v4, 1, v11
	s_waitcnt vmcnt(1)
	v_fmac_f32_e32 v3, v14, v9
	v_fmac_f32_e32 v10, v15, v8
	v_mul_f32_e32 v8, 0xbfb8aa3b, v10
	v_mul_f32_e32 v3, 0xbfb8aa3b, v3
	v_exp_f32_e32 v8, v8
	v_exp_f32_e32 v3, v3
	v_add_f32_e32 v8, 1.0, v8
	v_add_f32_e32 v3, 1.0, v3
	v_rcp_f32_e32 v8, v8
	v_rcp_f32_e32 v3, v3
	s_nop 0
	v_cvt_pk_bf16_f32 v3, v3, v8
	ds_write_b32 v4, v3
	s_and_saveexec_b64 s[8:9], vcc
	s_cbranch_execz .LBB0_1381
	v_mov_b32_e32 v7, 0
	v_lshl_add_u64 v[0:1], v[0:1], 0, v[6:7]
	v_mov_b32_e32 v7, v219
.LBB0_1381:
	s_or_b64 exec, exec, s[8:9]
	v_lshlrev_b32_e32 v0, 2, v5
	v_mov_b64_e32 v[8:9], v[238:239]
	v_readlane_b32 s49, v254, 23
	s_add_u32 s86, s74, 0x48480000
	s_waitcnt vmcnt(1)
	v_lshlrev_b32_e32 v12, 16, v2
	v_and_b32_e32 v13, 0xffff0000, v2
	v_and_b32_e32 v109, 15, v104
	v_ashrrev_i32_e32 v2, 4, v104
	s_movk_i32 s35, 0x190
	v_mov_b32_e32 v4, s49
	v_min_i32_e32 v14, 0x197, v104
	s_mov_b32 s36, 0x2aaaaaab
	v_add_u32_e32 v108, 64, v104
	v_readlane_b32 s48, v254, 24
	v_lshl_add_u32 v1, v5, 1, v11
	v_lshlrev_b32_e32 v20, 4, v104
	s_movk_i32 s6, 0x290
	s_addc_u32 s87, s75, 0
	v_lshlrev_b32_e32 v110, 3, v2
	v_or_b32_e32 v10, s48, v109
	v_mad_u32_u24 v177, v109, s35, v4
	v_mul_hi_i32 v4, v14, s36
	v_add_u32_e32 v11, 23, v14
	v_min_i32_e32 v15, 0x197, v108
	v_and_b32_e32 v5, 0xf0, v20
	s_add_u32 s88, s74, 0x33c80000
	v_ashrrev_i32_e32 v111, 31, v110
	v_mad_u32_u24 v30, v10, s6, 0
	v_lshrrev_b32_e32 v10, 31, v4
	v_ashrrev_i32_e32 v16, 2, v4
	v_cmp_gt_u32_e64 s[6:7], 47, v11
	v_mul_hi_i32 v11, v15, s36
	v_lshlrev_b32_e32 v6, 16, v7
	v_and_b32_e32 v7, 0xffff0000, v7
	s_mov_b64 s[10:11], 0x5e0000
	v_add_u32_e32 v21, s49, v5
	s_addc_u32 s89, s75, 0
	s_or_b32 s14, s33, s48
	v_lshl_add_u64 v[4:5], v[110:111], 1, s[74:75]
	v_add_u32_e32 v16, v16, v10
	v_lshrrev_b32_e32 v18, 31, v11
	v_ashrrev_i32_e32 v11, 2, v11
	v_pk_add_f32 v[6:7], v[6:7], v[12:13] neg_lo:[0,1] neg_hi:[0,1]
	v_lshl_add_u64 v[112:113], v[4:5], 0, s[10:11]
	s_and_b32 s10, s14, 0x7f0
	v_mul_lo_u32 v4, v16, 24
	v_add_u32_e32 v5, v11, v18
	v_or_b32_e32 v10, s14, v109
	s_cmp_eq_u32 s10, 0
	v_sub_u32_e32 v31, v14, v4
	v_mul_lo_u32 v4, v5, 24
	v_ashrrev_i32_e32 v11, 31, v10
	s_cselect_b64 s[38:39], -1, 0
	s_ashr_i32 s10, s14, 31
	v_sub_u32_e32 v32, v15, v4
	v_lshlrev_b64 v[114:115], 10, v[10:11]
	v_lshlrev_b32_e32 v11, 7, v31
	s_lshr_b32 s10, s10, 21
	v_and_b32_e32 v4, 0xfffffc00, v11
	v_add_u32_e32 v11, s10, v10
	v_ashrrev_i32_e32 v28, 11, v11
	v_mul_i32_i24_e32 v11, 0x800, v28
	v_sub_u32_e32 v29, v10, v11
	v_add_u32_e32 v22, 0xc0, v104
	v_add_u32_e32 v23, 0x100, v104
	v_add_u32_e32 v24, 0x140, v104
	v_add_u32_e32 v17, 23, v15
	v_cmp_gt_u32_e64 s[8:9], 47, v17
	s_and_b64 s[6:7], s[38:39], s[6:7]
	v_cndmask_b32_e64 v33, v16, 1, s[6:7]
	s_and_b64 s[6:7], s[38:39], s[8:9]
	v_cndmask_b32_e64 v34, v5, 1, s[6:7]
	v_add_u32_e32 v25, 0x180, v104
	s_waitcnt lgkmcnt(0)
	v_mov_b32_e32 v26, s13
	v_mov_b32_e32 v27, s5
	v_mov_b32_e32 v46, s12
	v_mov_b32_e32 v47, s4
	s_movk_i32 s4, 0x50
	v_lshlrev_b32_e32 v2, 2, v2
	s_add_i32 s33, s33, s48
	v_and_b32_e32 v0, -16, v104
	s_waitcnt vmcnt(0)
	v_pk_fma_f32 v[6:7], v[8:9], v[6:7], v[12:13]
	v_lshlrev_b32_e32 v3, 2, v104
	v_cvt_pk_bf16_f32 v6, v6, v7
	ds_write_b32 v1, v6
	v_lshlrev_b32_e32 v1, 7, v32
	v_and_b32_e32 v6, 0xfffffc00, v1
	v_add_u32_e32 v1, 0x80, v104
	v_min_i32_e32 v8, 0x197, v1
	v_mul_hi_i32 v9, v8, s36
	v_lshrrev_b32_e32 v10, 31, v9
	v_ashrrev_i32_e32 v9, 2, v9
	v_add_u32_e32 v9, v9, v10
	v_mul_lo_u32 v10, v9, 24
	v_sub_u32_e32 v35, v8, v10
	v_min_i32_e32 v10, 0x197, v22
	v_mul_hi_i32 v11, v10, s36
	v_lshrrev_b32_e32 v12, 31, v11
	v_ashrrev_i32_e32 v11, 2, v11
	v_add_u32_e32 v11, v11, v12
	v_mul_lo_u32 v12, v11, 24
	v_sub_u32_e32 v37, v10, v12
	v_min_i32_e32 v12, 0x197, v23
	v_mul_hi_i32 v13, v12, s36
	v_lshrrev_b32_e32 v14, 31, v13
	v_ashrrev_i32_e32 v13, 2, v13
	v_add_u32_e32 v13, v13, v14
	v_mul_lo_u32 v14, v13, 24
	v_sub_u32_e32 v39, v12, v14
	v_min_i32_e32 v14, 0x197, v24
	v_mul_hi_i32 v15, v14, s36
	v_add_u32_e32 v8, 23, v8
	v_lshrrev_b32_e32 v16, 31, v15
	v_ashrrev_i32_e32 v15, 2, v15
	v_cmp_gt_u32_e64 s[6:7], 47, v8
	v_add_u32_e32 v15, v15, v16
	s_and_b64 s[6:7], s[38:39], s[6:7]
	v_add_u32_e32 v10, 23, v10
	v_mul_lo_u32 v16, v15, 24
	v_cndmask_b32_e64 v36, v9, 1, s[6:7]
	v_cmp_gt_u32_e64 s[6:7], 47, v10
	v_sub_u32_e32 v41, v14, v16
	v_min_i32_e32 v16, 0x197, v25
	s_and_b64 s[6:7], s[38:39], s[6:7]
	v_add_u32_e32 v12, 23, v12
	v_mul_hi_i32 v17, v16, s36
	v_cndmask_b32_e64 v38, v11, 1, s[6:7]
	v_cmp_gt_u32_e64 s[6:7], 47, v12
	v_lshrrev_b32_e32 v18, 31, v17
	v_ashrrev_i32_e32 v17, 2, v17
	s_and_b64 s[6:7], s[38:39], s[6:7]
	v_add_u32_e32 v14, 23, v14
	v_add_u32_e32 v17, v17, v18
	v_cndmask_b32_e64 v40, v13, 1, s[6:7]
	v_cmp_gt_u32_e64 s[6:7], 47, v14
	v_mul_lo_u32 v18, v17, 24
	s_and_b64 s[6:7], s[38:39], s[6:7]
	v_sub_u32_e32 v43, v16, v18
	v_add_u32_e32 v16, 23, v16
	v_cndmask_b32_e64 v42, v15, 1, s[6:7]
	v_cmp_gt_u32_e64 s[6:7], 47, v16
	s_and_b64 s[6:7], s[38:39], s[6:7]
	v_xor_b32_e32 v178, 64, v3
	v_cndmask_b32_e64 v44, v17, 1, s[6:7]
	s_movk_i32 s6, 0x90
	v_cmp_gt_i32_e64 s[6:7], s6, v104
	v_xor_b32_e32 v179, 0x80, v3
	v_ashrrev_i32_e32 v3, 31, v2
	v_cndmask_b32_e64 v45, 0, v104, s[6:7]
	v_ashrrev_i32_e32 v180, 4, v45
	v_cmp_eq_u32_e64 s[10:11], 7, v180
	v_lshlrev_b32_e32 v18, 10, v180
	v_ashrrev_i32_e32 v19, 31, v18
	v_cndmask_b32_e64 v117, v26, v27, s[10:11]
	v_cndmask_b32_e64 v116, v46, v47, s[10:11]
	v_cmp_gt_i32_e64 s[10:11], s4, v104
	v_lshl_add_u64 v[118:119], v[18:19], 2, s[40:41]
	s_movk_i32 s4, 0x198
	v_cndmask_b32_e64 v48, 0, v108, s[10:11]
	v_ashrrev_i32_e32 v181, 4, v48
	v_cmp_eq_u32_e64 s[14:15], 7, v181
	v_lshlrev_b32_e32 v18, 10, v181
	v_ashrrev_i32_e32 v19, 31, v18
	v_cndmask_b32_e64 v121, v26, v27, s[14:15]
	v_cndmask_b32_e64 v120, v46, v47, s[14:15]
	v_cmp_gt_i32_e64 s[14:15], 16, v104
	v_lshl_add_u64 v[122:123], v[18:19], 2, s[40:41]
	v_ashrrev_i32_e32 v5, 31, v4
	v_cndmask_b32_e64 v49, 0, v1, s[14:15]
	v_ashrrev_i32_e32 v182, 4, v49
	v_lshlrev_b32_e32 v18, 10, v182
	v_ashrrev_i32_e32 v19, 31, v18
	v_lshl_add_u64 v[126:127], v[18:19], 2, s[40:41]
	v_mul_hi_i32 v18, v104, s36
	v_lshrrev_b32_e32 v19, 31, v18
	v_ashrrev_i32_e32 v18, 2, v18
	v_add_u32_e32 v18, v18, v19
	v_mul_lo_u32 v19, v18, 24
	v_cmp_eq_u32_e64 s[18:19], 7, v182
	v_sub_u32_e32 v19, v104, v19
	v_lshlrev_b32_e32 v19, 4, v19
	v_cndmask_b32_e64 v125, v26, v27, s[18:19]
	v_add_u32_e32 v26, 23, v104
	v_cmp_gt_u32_e64 s[20:21], 47, v26
	v_mul_lo_u32 v18, v18, s35
	v_and_b32_e32 v26, 0xffffff80, v19
	v_cndmask_b32_e64 v124, v46, v47, s[18:19]
	v_add3_u32 v46, s49, v18, v26
	v_mul_hi_i32 v18, v108, s36
	v_and_b32_e32 v47, 0x70, v19
	v_lshrrev_b32_e32 v19, 31, v18
	v_ashrrev_i32_e32 v18, 2, v18
	v_add_u32_e32 v18, v18, v19
	v_mul_lo_u32 v19, v18, 24
	v_sub_u32_e32 v19, v108, v19
	v_add_u32_e32 v26, 0x57, v104
	v_lshlrev_b32_e32 v19, 4, v19
	v_cmp_gt_u32_e64 s[22:23], 47, v26
	v_mul_lo_u32 v18, v18, s35
	v_and_b32_e32 v26, 0xffffff80, v19
	v_add3_u32 v50, s49, v18, v26
	v_mul_hi_i32 v18, v1, s36
	v_and_b32_e32 v51, 0x70, v19
	v_lshrrev_b32_e32 v19, 31, v18
	v_ashrrev_i32_e32 v18, 2, v18
	v_add_u32_e32 v18, v18, v19
	v_mul_lo_u32 v19, v18, 24
	v_sub_u32_e32 v19, v1, v19
	v_add_u32_e32 v26, 0x97, v104
	v_lshlrev_b32_e32 v19, 4, v19
	v_cmp_gt_u32_e64 s[24:25], 47, v26
	v_mul_lo_u32 v18, v18, s35
	v_and_b32_e32 v26, 0xffffff80, v19
	v_add3_u32 v52, s49, v18, v26
	v_mul_hi_i32 v18, v22, s36
	v_and_b32_e32 v53, 0x70, v19
	v_lshrrev_b32_e32 v19, 31, v18
	v_ashrrev_i32_e32 v18, 2, v18
	v_add_u32_e32 v18, v18, v19
	v_mul_lo_u32 v19, v18, 24
	v_sub_u32_e32 v19, v22, v19
	v_add_u32_e32 v22, 0xd7, v104
	v_lshlrev_b32_e32 v19, 4, v19
	v_cmp_gt_u32_e64 s[26:27], 47, v22
	v_mul_lo_u32 v18, v18, s35
	v_and_b32_e32 v22, 0xffffff80, v19
	v_add3_u32 v54, s49, v18, v22
	v_mul_hi_i32 v18, v23, s36
	v_and_b32_e32 v55, 0x70, v19
	v_lshrrev_b32_e32 v19, 31, v18
	v_ashrrev_i32_e32 v18, 2, v18
	v_add_u32_e32 v18, v18, v19
	v_mul_lo_u32 v19, v18, 24
	v_sub_u32_e32 v19, v23, v19
	v_add_u32_e32 v22, 0x117, v104
	v_lshlrev_b32_e32 v19, 4, v19
	v_cmp_gt_u32_e64 s[28:29], 47, v22
	v_mul_lo_u32 v18, v18, s35
	v_and_b32_e32 v22, 0xffffff80, v19
	v_add3_u32 v56, s49, v18, v22
	v_mul_hi_i32 v18, v24, s36
	v_and_b32_e32 v57, 0x70, v19
	v_lshrrev_b32_e32 v19, 31, v18
	v_ashrrev_i32_e32 v18, 2, v18
	v_add_u32_e32 v18, v18, v19
	v_mul_lo_u32 v19, v18, 24
	v_sub_u32_e32 v19, v24, v19
	v_add_u32_e32 v22, 0x157, v104
	v_lshlrev_b32_e32 v19, 4, v19
	v_cmp_gt_u32_e64 s[30:31], 47, v22
	v_mul_lo_u32 v18, v18, s35
	v_and_b32_e32 v22, 0xffffff80, v19
	v_add3_u32 v58, s49, v18, v22
	v_mul_hi_i32 v18, v25, s36
	v_and_b32_e32 v59, 0x70, v19
	v_lshrrev_b32_e32 v19, 31, v18
	v_ashrrev_i32_e32 v18, 2, v18
	v_add_u32_e32 v18, v18, v19
	v_mul_lo_u32 v19, v18, 24
	v_sub_u32_e32 v19, v25, v19
	v_cmp_gt_i32_e64 s[18:19], s4, v104
	s_movk_i32 s4, 0x158
	v_add_u32_e32 v22, 0x197, v104
	v_lshlrev_b32_e32 v19, 4, v19
	s_and_b64 s[40:41], s[20:21], s[38:39]
	v_cmp_gt_i32_e64 s[20:21], s4, v104
	s_movk_i32 s4, 0x118
	v_cmp_gt_u32_e64 s[36:37], 47, v22
	v_mul_lo_u32 v18, v18, s35
	v_and_b32_e32 v22, 0xffffff80, v19
	s_and_b64 s[90:91], s[22:23], s[38:39]
	v_cmp_gt_i32_e64 s[22:23], s4, v104
	s_movk_i32 s4, 0xd8
	v_add3_u32 v60, s49, v18, v22
	v_and_b32_e32 v18, 0xffffff00, v20
	s_and_b64 s[92:93], s[24:25], s[38:39]
	v_cmp_gt_i32_e64 s[24:25], s4, v104
	s_movk_i32 s4, 0x98
	v_add_u32_e32 v183, v21, v18
	v_lshlrev_b32_e32 v18, 4, v108
	s_and_b64 s[94:95], s[26:27], s[38:39]
	v_cmp_gt_i32_e64 s[26:27], s4, v104
	s_movk_i32 s4, 0x58
	v_and_b32_e32 v18, 0xffffff00, v18
	v_add_u32_e32 v24, 16, v2
	s_and_b64 s[96:97], s[28:29], s[38:39]
	v_cmp_gt_i32_e64 s[28:29], s4, v104
	s_and_b64 s[4:5], s[30:31], s[38:39]
	s_and_b64 s[62:63], s[36:37], s[38:39]
	v_add_u32_e32 v184, v21, v18
	v_lshlrev_b32_e32 v18, 2, v24
	v_add_u32_e32 v25, 32, v2
	v_lshlrev_b32_e32 v62, 1, v24
	v_add_u32_e32 v24, s33, v109
	v_readlane_b32 s35, v254, 25
	v_lshlrev_b32_e32 v20, 2, v25
	v_add_u32_e32 v26, 48, v2
	v_lshlrev_b32_e32 v63, 1, v25
	v_ashrrev_i32_e32 v25, 31, v24
	s_add_u32 s36, s80, s35
	v_lshlrev_b32_e32 v22, 2, v26
	v_lshlrev_b32_e32 v64, 1, v26
	v_lshlrev_b64 v[26:27], 6, v[24:25]
	s_addc_u32 s37, s81, 0
	v_readlane_b32 s35, v254, 26
	v_lshl_add_u64 v[26:27], s[36:37], 0, v[26:27]
	s_mov_b64 s[36:37], 0x4c0000
	v_lshl_add_u32 v28, v28, 4, s35
	s_movk_i32 s35, 0x300
	v_lshl_add_u64 v[128:129], v[26:27], 0, s[36:37]
	v_mad_i64_i32 v[26:27], s[36:37], v29, s35, 0
	s_mov_b32 s35, 0x180000
	v_lshlrev_b32_e32 v1, 4, v1
	v_mad_i64_i32 v[26:27], s[36:37], v28, s35, v[26:27]
	v_and_b32_e32 v1, 0xffffff00, v1
	v_lshl_add_u64 v[28:29], v[26:27], 0, v[110:111]
	v_add_u32_e32 v185, v21, v1
	v_ashrrev_i32_e32 v1, 31, v0
	v_lshl_add_u64 v[28:29], s[80:81], 0, v[28:29]
	s_mov_b64 s[36:37], 0x3e480140
	v_and_b32_e32 v61, 0x70, v19
	v_ashrrev_i32_e32 v19, 31, v18
	v_lshl_add_u64 v[130:131], v[28:29], 0, s[36:37]
	v_lshl_add_u64 v[28:29], v[26:27], 0, v[0:1]
	v_add_u32_e32 v111, s64, v2
	v_lshl_add_u64 v[28:29], s[80:81], 0, v[28:29]
	s_mov_b64 s[38:39], 0x3e480000
	v_lshl_add_u64 v[18:19], v[26:27], 0, v[18:19]
	v_lshlrev_b64 v[2:3], 1, v[2:3]
	v_lshl_add_u64 v[132:133], v[28:29], 0, s[38:39]
	v_sub_co_u32_e64 v28, s[36:37], v18, v2
	v_ashrrev_i32_e32 v21, 31, v20
	s_nop 0
	v_subb_co_u32_e64 v29, s[36:37], v19, v3, s[36:37]
	v_lshl_add_u64 v[18:19], s[80:81], 0, v[18:19]
	v_lshl_add_u64 v[136:137], v[18:19], 0, s[38:39]
	v_lshl_add_u64 v[18:19], v[26:27], 0, v[20:21]
	v_sub_co_u32_e64 v20, s[36:37], v18, v2
	v_ashrrev_i32_e32 v23, 31, v22
	s_nop 0
	v_subb_co_u32_e64 v21, s[36:37], v19, v3, s[36:37]
	v_lshl_add_u64 v[18:19], s[80:81], 0, v[18:19]
	v_lshl_add_u64 v[140:141], v[18:19], 0, s[38:39]
	v_lshl_add_u64 v[18:19], v[26:27], 0, v[22:23]
	v_lshl_add_u64 v[138:139], s[80:81], 0, v[20:21]
	v_sub_co_u32_e64 v20, s[36:37], v18, v2
	v_add3_u32 v1, s33, v33, -1
	s_nop 0
	v_subb_co_u32_e64 v21, s[36:37], v19, v3, s[36:37]
	v_lshl_add_u64 v[18:19], s[80:81], 0, v[18:19]
	s_movk_i32 s35, 0x3400
	v_lshl_add_u64 v[144:145], v[18:19], 0, s[38:39]
	v_mad_i64_i32 v[18:19], s[36:37], v1, s35, 0
	v_and_b32_e32 v1, 7, v31
	v_readlane_b32 s36, v254, 27
	v_lshl_or_b32 v18, v1, 4, v18
	v_readlane_b32 s37, v254, 28
	s_add_u32 s36, s80, s36
	v_lshl_add_u64 v[4:5], v[4:5], 1, v[18:19]
	s_addc_u32 s37, s81, s37
	v_lshl_add_u64 v[4:5], s[36:37], 0, v[4:5]
	s_mov_b64 s[38:39], 0x37c80000
	v_add3_u32 v1, s33, v34, -1
	v_add_u32_e32 v107, s49, v0
	v_lshl_add_u64 v[146:147], v[4:5], 0, s[38:39]
	v_mad_i64_i32 v[4:5], s[48:49], v1, s35, 0
	v_and_b32_e32 v1, 7, v32
	v_ashrrev_i32_e32 v7, 31, v6
	v_lshl_or_b32 v4, v1, 4, v4
	v_lshl_add_u64 v[4:5], v[6:7], 1, v[4:5]
	v_lshlrev_b32_e32 v8, 7, v35
	v_lshl_add_u64 v[4:5], s[36:37], 0, v[4:5]
	v_add3_u32 v1, s33, v36, -1
	v_and_b32_e32 v8, 0xfffffc00, v8
	v_lshl_add_u64 v[148:149], v[4:5], 0, s[38:39]
	v_mad_i64_i32 v[4:5], s[48:49], v1, s35, 0
	v_and_b32_e32 v1, 7, v35
	v_ashrrev_i32_e32 v9, 31, v8
	v_lshl_or_b32 v4, v1, 4, v4
	v_lshl_add_u64 v[4:5], v[8:9], 1, v[4:5]
	v_lshlrev_b32_e32 v10, 7, v37
	v_lshl_add_u64 v[4:5], s[36:37], 0, v[4:5]
	v_add3_u32 v1, s33, v38, -1
	v_and_b32_e32 v10, 0xfffffc00, v10
	v_lshl_add_u64 v[150:151], v[4:5], 0, s[38:39]
	v_mad_i64_i32 v[4:5], s[48:49], v1, s35, 0
	v_and_b32_e32 v1, 7, v37
	v_ashrrev_i32_e32 v11, 31, v10
	v_lshl_or_b32 v4, v1, 4, v4
	v_lshl_add_u64 v[4:5], v[10:11], 1, v[4:5]
	v_lshlrev_b32_e32 v12, 7, v39
	v_lshl_add_u64 v[4:5], s[36:37], 0, v[4:5]
	v_add3_u32 v1, s33, v40, -1
	v_and_b32_e32 v12, 0xfffffc00, v12
	v_lshl_add_u64 v[152:153], v[4:5], 0, s[38:39]
	v_mad_i64_i32 v[4:5], s[48:49], v1, s35, 0
	v_and_b32_e32 v1, 7, v39
	v_ashrrev_i32_e32 v13, 31, v12
	v_lshl_or_b32 v4, v1, 4, v4
	v_lshl_add_u64 v[4:5], v[12:13], 1, v[4:5]
	v_lshlrev_b32_e32 v14, 7, v41
	v_lshl_add_u64 v[4:5], s[36:37], 0, v[4:5]
	v_add3_u32 v1, s33, v42, -1
	v_and_b32_e32 v14, 0xfffffc00, v14
	v_lshl_add_u64 v[154:155], v[4:5], 0, s[38:39]
	v_mad_i64_i32 v[4:5], s[48:49], v1, s35, 0
	v_and_b32_e32 v1, 7, v41
	v_ashrrev_i32_e32 v15, 31, v14
	v_lshl_or_b32 v4, v1, 4, v4
	v_lshl_add_u64 v[4:5], v[14:15], 1, v[4:5]
	v_lshlrev_b32_e32 v16, 7, v43
	v_lshl_add_u64 v[4:5], s[36:37], 0, v[4:5]
	v_add3_u32 v1, s33, v44, -1
	v_and_b32_e32 v16, 0xfffffc00, v16
	v_lshl_add_u64 v[156:157], v[4:5], 0, s[38:39]
	v_mad_i64_i32 v[4:5], s[48:49], v1, s35, 0
	v_and_b32_e32 v1, 7, v43
	v_ashrrev_i32_e32 v17, 31, v16
	v_lshl_or_b32 v4, v1, 4, v4
	v_lshl_add_u64 v[4:5], v[16:17], 1, v[4:5]
	v_lshl_add_u64 v[4:5], s[36:37], 0, v[4:5]
	v_lshl_add_u64 v[158:159], v[4:5], 0, s[38:39]
	v_and_b32_e32 v1, 15, v45
	v_readlane_b32 s38, v254, 29
	v_lshlrev_b32_e32 v4, 4, v1
	v_mov_b32_e32 v5, 0
	v_readlane_b32 s39, v254, 30
	v_and_b32_e32 v1, 15, v48
	s_mov_b32 s79, 0
	v_lshl_add_u64 v[160:161], v[4:5], 0, s[38:39]
	v_lshlrev_b32_e32 v4, 4, v1
	v_and_b32_e32 v1, 15, v49
	v_lshl_add_u64 v[162:163], v[4:5], 0, s[38:39]
	v_lshlrev_b32_e32 v4, 4, v1
	v_lshl_add_u64 v[164:165], v[4:5], 0, s[38:39]
	v_lshlrev_b64 v[4:5], 11, v[24:25]
	v_lshl_add_u64 v[2:3], v[4:5], 0, v[2:3]
	v_lshl_add_u64 v[2:3], s[36:37], 0, v[2:3]
	s_mov_b64 s[36:37], 0x4a480040
	v_cmp_gt_u32_e32 vcc, 16, v104
	v_cmp_lt_i32_e64 s[8:9], 2, v180
	v_cmp_lt_i32_e64 s[12:13], 2, v181
	v_cmp_lt_i32_e64 s[16:17], 2, v182
	v_cmp_gt_i32_e64 s[30:31], 24, v104
	v_add_u32_e32 v186, s64, v109
	v_lshl_add_u64 v[134:135], s[80:81], 0, v[28:29]
	v_lshl_add_u64 v[142:143], s[80:81], 0, v[20:21]
	v_lshl_add_u64 v[166:167], v[2:3], 0, s[36:37]
	s_movk_i32 s57, 0x280
	v_add_u32_e32 v187, v46, v47
	v_add_u32_e32 v188, v50, v51
	v_add_u32_e32 v189, v52, v53
	v_add_u32_e32 v190, v54, v55
	v_add_u32_e32 v191, v56, v57
	v_add_u32_e32 v192, v58, v59
	v_add_u32_e32 v193, v60, v61
	s_mov_b32 s35, 0xc1a00000
	s_mov_b32 s50, 0x800000
	s_mov_b32 s51, 0x3f317217
	s_mov_b32 s33, 0x7f800000
	s_mov_b32 s52, 0x3e480000
	s_mov_b64 s[64:65], 0x180000
	s_mov_b64 s[66:67], 0x80
	s_mov_b64 s[68:69], 0x100
	v_add_u32_e32 v194, v30, v0
	v_mov_b32_e32 v195, 0x41b17218
	v_add_u32_e32 v196, v177, v62
	v_add_u32_e32 v197, v177, v63
	v_add_u32_e32 v198, v177, v64
	s_waitcnt lgkmcnt(0)
	s_barrier
	s_branch .LBB0_1383
